# speedup vs baseline: 1.0403x; 1.0143x over previous
_Z9ssim_mainPKfS0_S0_Pf:
	v_readfirstlane_b32 s29, v0
	s_load_dwordx4 s[4:7], s[0:1], 0x0
	s_load_dwordx4 s[8:11], s[0:1], 0x10
	s_mov_b32 s51, 0x44800000
	s_mov_b32 s38, 0
	s_mov_b32 s39, -1
	s_lshr_b32 s12, s29, 6
	s_and_b32 s13, s2, 7
	s_lshl_b32 s13, s13, 5
	s_lshr_b32 s14, s2, 3
	s_add_u32 s13, s13, s14
	s_lshr_b32 s14, s13, 3
	s_and_b32 s15, s13, 7
	s_lshl_b32 s16, s14, 20
	s_lshl_b32 s17, s15, 17
	s_add_u32 s16, s16, s17
	s_lshl_b32 s17, s12, 8
	s_add_u32 s16, s16, s17
	s_lshl_b32 s27, s12, 2
	s_add_u32 s27, s27, 0x10000
	v_and_b32_e32 v8, 63, v0
	v_and_b32_e32 v169, 15, v0
	v_bfe_u32 v164, v0, 4, 2
	v_mov_b32_e32 v6, s27
	v_mov_b32_e32 v168, 0
	ds_write_b32 v6, v168 offset:0
	ds_write_b32 v6, v168 offset:32
	ds_write_b32 v6, v168 offset:64
	ds_write_b32 v6, v168 offset:96
	v_lshrrev_b32_e32 v167, 2, v169
	v_lshlrev_b32_e32 v167, 5, v167
	v_and_b32_e32 v168, 1, v169
	v_lshl_or_b32 v167, v168, 4, v167
	v_bfe_u32 v168, v169, 1, 1
	v_lshl_or_b32 v167, v168, 7, v167
	v_lshl_or_b32 v9, v164, 14, v167
	v_and_b32_e32 v168, 1, v164
	v_lshl_or_b32 v23, v168, 14, v167
	v_lshrrev_b32_e32 v168, 1, v164
	v_lshl_or_b32 v23, v168, 13, v23
	v_add_u32_e32 v237, 0x1000, v9
	v_add_u32_e32 v238, 0x2000, v9
	v_add_u32_e32 v239, 0x3000, v9
	v_add_u32_e32 v240, 0x10000, v9
	v_add_u32_e32 v241, 0x11000, v9
	v_add_u32_e32 v242, 0x12000, v9
	v_add_u32_e32 v243, 0x13000, v9
	s_waitcnt lgkmcnt(0)
	s_add_u32 s18, s4, s16
	s_addc_u32 s19, s5, 0
	s_add_u32 s20, s6, s16
	s_addc_u32 s21, s7, 0
	global_load_dwordx4 v[36:39], v9, s[18:19] offset:0 sc1 nt
	global_load_dwordx4 v[40:43], v9, s[18:19] offset:2048 sc1 nt
	global_load_dwordx4 v[68:71], v9, s[20:21] offset:0 sc1 nt
	global_load_dwordx4 v[72:75], v9, s[20:21] offset:2048 sc1 nt
	global_load_dwordx4 v[44:47], v237, s[18:19] offset:0 sc1 nt
	global_load_dwordx4 v[48:51], v237, s[18:19] offset:2048 sc1 nt
	global_load_dwordx4 v[76:79], v237, s[20:21] offset:0 sc1 nt
	global_load_dwordx4 v[80:83], v237, s[20:21] offset:2048 sc1 nt
	global_load_dwordx4 v[52:55], v238, s[18:19] offset:0 sc1 nt
	global_load_dwordx4 v[56:59], v238, s[18:19] offset:2048 sc1 nt
	global_load_dwordx4 v[84:87], v238, s[20:21] offset:0 sc1 nt
	global_load_dwordx4 v[88:91], v238, s[20:21] offset:2048 sc1 nt
	global_load_dwordx4 v[60:63], v239, s[18:19] offset:0 sc1 nt
	global_load_dwordx4 v[64:67], v239, s[18:19] offset:2048 sc1 nt
	global_load_dwordx4 v[92:95], v239, s[20:21] offset:0 sc1 nt
	global_load_dwordx4 v[96:99], v239, s[20:21] offset:2048 sc1 nt
	v_lshlrev_b32_e32 v167, 3, v164
	v_xor_b32_e32 v168, 16, v167
	v_sub_u32_e32 v165, v167, v169
	v_sub_u32_e32 v166, v168, v169
	v_add_u32_e32 v172, 0, v165
	v_med3_i32 v172, v172, 0, 10
	v_lshlrev_b32_e32 v172, 2, v172
	v_add_u32_e32 v173, 1, v165
	v_med3_i32 v173, v173, 0, 10
	v_lshlrev_b32_e32 v173, 2, v173
	v_add_u32_e32 v174, 2, v165
	v_med3_i32 v174, v174, 0, 10
	v_lshlrev_b32_e32 v174, 2, v174
	v_add_u32_e32 v175, 3, v165
	v_med3_i32 v175, v175, 0, 10
	v_lshlrev_b32_e32 v175, 2, v175
	v_add_u32_e32 v176, 4, v165
	v_med3_i32 v176, v176, 0, 10
	v_lshlrev_b32_e32 v176, 2, v176
	v_add_u32_e32 v177, 5, v165
	v_med3_i32 v177, v177, 0, 10
	v_lshlrev_b32_e32 v177, 2, v177
	v_add_u32_e32 v178, 6, v165
	v_med3_i32 v178, v178, 0, 10
	v_lshlrev_b32_e32 v178, 2, v178
	v_add_u32_e32 v179, 7, v165
	v_med3_i32 v179, v179, 0, 10
	v_lshlrev_b32_e32 v179, 2, v179
	v_add_u32_e32 v180, 0, v166
	v_med3_i32 v180, v180, 0, 10
	v_lshlrev_b32_e32 v180, 2, v180
	v_add_u32_e32 v181, 1, v166
	v_med3_i32 v181, v181, 0, 10
	v_lshlrev_b32_e32 v181, 2, v181
	v_add_u32_e32 v182, 2, v166
	v_med3_i32 v182, v182, 0, 10
	v_lshlrev_b32_e32 v182, 2, v182
	v_add_u32_e32 v183, 3, v166
	v_med3_i32 v183, v183, 0, 10
	v_lshlrev_b32_e32 v183, 2, v183
	v_add_u32_e32 v184, 4, v166
	v_med3_i32 v184, v184, 0, 10
	v_lshlrev_b32_e32 v184, 2, v184
	v_add_u32_e32 v185, 5, v166
	v_med3_i32 v185, v185, 0, 10
	v_lshlrev_b32_e32 v185, 2, v185
	v_add_u32_e32 v186, 6, v166
	v_med3_i32 v186, v186, 0, 10
	v_lshlrev_b32_e32 v186, 2, v186
	v_add_u32_e32 v187, 7, v166
	v_med3_i32 v187, v187, 0, 10
	v_lshlrev_b32_e32 v187, 2, v187
	s_load_dwordx8 s[40:47], s[8:9], 0x0
	s_load_dwordx2 s[48:49], s[8:9], 0x20
	s_load_dword s50, s[8:9], 0x28
	global_load_dwordx4 v[100:103], v240, s[18:19] offset:0 sc1 nt
	global_load_dwordx4 v[104:107], v240, s[18:19] offset:2048 sc1 nt
	global_load_dwordx4 v[132:135], v240, s[20:21] offset:0 sc1 nt
	global_load_dwordx4 v[136:139], v240, s[20:21] offset:2048 sc1 nt
	global_load_dwordx4 v[108:111], v241, s[18:19] offset:0 sc1 nt
	global_load_dwordx4 v[112:115], v241, s[18:19] offset:2048 sc1 nt
	global_load_dwordx4 v[140:143], v241, s[20:21] offset:0 sc1 nt
	global_load_dwordx4 v[144:147], v241, s[20:21] offset:2048 sc1 nt
	global_load_dwordx4 v[116:119], v242, s[18:19] offset:0 sc1 nt
	global_load_dwordx4 v[120:123], v242, s[18:19] offset:2048 sc1 nt
	global_load_dwordx4 v[148:151], v242, s[20:21] offset:0 sc1 nt
	global_load_dwordx4 v[152:155], v242, s[20:21] offset:2048 sc1 nt
	global_load_dwordx4 v[124:127], v243, s[18:19] offset:0 sc1 nt
	global_load_dwordx4 v[128:131], v243, s[18:19] offset:2048 sc1 nt
	global_load_dwordx4 v[156:159], v243, s[20:21] offset:0 sc1 nt
	global_load_dwordx4 v[160:163], v243, s[20:21] offset:2048 sc1 nt
	s_cmp_eq_u32 s15, 7
	s_cselect_b32 s22, 0, 0x20000
	s_add_u32 s84, s18, s22
	s_addc_u32 s85, s19, 0
	s_add_u32 s86, s18, s22
	s_addc_u32 s87, s19, 0
	s_add_u32 s86, s86, 0x1000
	s_addc_u32 s87, s87, 0
	s_add_u32 s88, s20, s22
	s_addc_u32 s89, s21, 0
	s_add_u32 s90, s20, s22
	s_addc_u32 s91, s21, 0
	s_add_u32 s90, s90, 0x1000
	s_addc_u32 s91, s91, 0
	s_waitcnt lgkmcnt(0)
	v_writelane_b32 v171, s40, 0
	v_writelane_b32 v171, s41, 1
	v_writelane_b32 v171, s42, 2
	v_writelane_b32 v171, s43, 3
	v_writelane_b32 v171, s44, 4
	v_writelane_b32 v171, s45, 5
	v_writelane_b32 v171, s46, 6
	v_writelane_b32 v171, s47, 7
	v_writelane_b32 v171, s48, 8
	v_writelane_b32 v171, s49, 9
	v_writelane_b32 v171, s50, 10
	ds_bpermute_b32 v188, v172, v171
	ds_bpermute_b32 v189, v173, v171
	ds_bpermute_b32 v190, v174, v171
	ds_bpermute_b32 v191, v175, v171
	ds_bpermute_b32 v192, v176, v171
	ds_bpermute_b32 v193, v177, v171
	ds_bpermute_b32 v194, v178, v171
	ds_bpermute_b32 v195, v179, v171
	s_waitcnt lgkmcnt(0)
	ds_bpermute_b32 v196, v180, v171
	ds_bpermute_b32 v197, v181, v171
	ds_bpermute_b32 v198, v182, v171
	ds_bpermute_b32 v199, v183, v171
	ds_bpermute_b32 v200, v184, v171
	ds_bpermute_b32 v201, v185, v171
	ds_bpermute_b32 v202, v186, v171
	ds_bpermute_b32 v203, v187, v171
	v_mov_b32_e32 v229, 0x44800000
	v_fma_mixlo_f16 v228, s40, v229, 0
	v_cvt_f32_f16_e32 v228, v228
	v_cvt_f64_f32_e32 v[212:213], v228
	v_add_f64 v[212:213], v[212:213], 0
	v_fma_mixlo_f16 v228, s41, v229, 0
	v_cvt_f32_f16_e32 v228, v228
	v_cvt_f64_f32_e32 v[214:215], v228
	v_add_f64 v[212:213], v[212:213], v[214:215]
	v_fma_mixlo_f16 v228, s42, v229, 0
	v_cvt_f32_f16_e32 v228, v228
	v_cvt_f64_f32_e32 v[214:215], v228
	v_add_f64 v[212:213], v[212:213], v[214:215]
	v_fma_mixlo_f16 v228, s43, v229, 0
	v_cvt_f32_f16_e32 v228, v228
	v_cvt_f64_f32_e32 v[214:215], v228
	v_add_f64 v[212:213], v[212:213], v[214:215]
	v_fma_mixlo_f16 v228, s44, v229, 0
	v_cvt_f32_f16_e32 v228, v228
	v_cvt_f64_f32_e32 v[214:215], v228
	v_add_f64 v[212:213], v[212:213], v[214:215]
	v_fma_mixlo_f16 v228, s45, v229, 0
	v_cvt_f32_f16_e32 v228, v228
	v_cvt_f64_f32_e32 v[214:215], v228
	v_add_f64 v[212:213], v[212:213], v[214:215]
	v_fma_mixlo_f16 v228, s46, v229, 0
	v_cvt_f32_f16_e32 v228, v228
	v_cvt_f64_f32_e32 v[214:215], v228
	v_add_f64 v[212:213], v[212:213], v[214:215]
	v_fma_mixlo_f16 v228, s47, v229, 0
	v_cvt_f32_f16_e32 v228, v228
	v_cvt_f64_f32_e32 v[214:215], v228
	v_add_f64 v[212:213], v[212:213], v[214:215]
	v_fma_mixlo_f16 v228, s48, v229, 0
	v_cvt_f32_f16_e32 v228, v228
	v_cvt_f64_f32_e32 v[214:215], v228
	v_add_f64 v[212:213], v[212:213], v[214:215]
	v_fma_mixlo_f16 v228, s49, v229, 0
	v_cvt_f32_f16_e32 v228, v228
	v_cvt_f64_f32_e32 v[214:215], v228
	v_add_f64 v[212:213], v[212:213], v[214:215]
	v_fma_mixlo_f16 v228, s50, v229, 0
	v_cvt_f32_f16_e32 v228, v228
	v_cvt_f64_f32_e32 v[214:215], v228
	v_add_f64 v[212:213], v[212:213], v[214:215]
	v_mul_f64 v[212:213], v[212:213], v[212:213]
	v_mul_f64 v[216:217], v[212:213], 0.5
	v_add_f64 v[218:219], v[216:217], v[216:217]
	s_mov_b32 s36, 0xeb1c432d
	s_mov_b32 s37, 0x3f1a36e2
	v_mul_f64 v[220:221], v[212:213], s[36:37]
	v_mul_f64 v[222:223], v[216:217], v[218:219]
	v_fmac_f64_e32 v[222:223], v[212:213], v[220:221]
	v_add_f64 v[224:225], v[212:213], v[212:213]
	s_mov_b32 s36, 0x487fcb92
	s_mov_b32 s37, 0x3f4d7dbf
	v_mul_f64 v[226:227], v[212:213], s[36:37]
	v_cvt_f32_f64_e32 v0, v[226:227]
	v_mov_b32_e32 v1, v0
	v_mov_b32_e32 v2, v0
	v_mov_b32_e32 v3, v0
	v_cvt_f32_f64_e32 v10, v[218:219]
	v_cvt_f32_f64_e32 v11, v[222:223]
	v_cvt_f32_f64_e32 v12, v[212:213]
	v_cvt_f32_f64_e32 v13, v[224:225]
	v_mul_f64 v[226:227], v[212:213], v[226:227]
	v_cvt_f32_f64_e32 v14, v[226:227]
	v_lshlrev_b32_e32 v167, 2, v164
	s_cmp_eq_u32 s12, 0
	s_cselect_b32 s23, 6, 64
	v_add_u32_e32 v168, 0, v167
	v_cmp_gt_u32_e32 vcc, s23, v168
	s_nop 1
	v_cndmask_b32_e64 v15, 0, 1.0, vcc
	v_add_u32_e32 v168, 1, v167
	v_cmp_gt_u32_e32 vcc, s23, v168
	s_nop 1
	v_cndmask_b32_e64 v16, 0, 1.0, vcc
	v_add_u32_e32 v168, 2, v167
	v_cmp_gt_u32_e32 vcc, s23, v168
	s_nop 1
	v_cndmask_b32_e64 v17, 0, 1.0, vcc
	v_add_u32_e32 v168, 3, v167
	v_cmp_gt_u32_e32 vcc, s23, v168
	s_nop 1
	v_cndmask_b32_e64 v18, 0, 1.0, vcc
	v_and_b32_e32 v167, 31, v8
	v_lshlrev_b32_e32 v167, 4, v167
	s_lshl_b32 s24, s12, 11
	s_add_i32 s25, s12, 7
	s_and_b32 s25, s25, 7
	s_lshl_b32 s26, s25, 11
	v_or_b32_e32 v4, s24, v167
	v_or_b32_e32 v5, s26, v167
	s_lshl_b32 s28, s25, 2
	s_add_u32 s28, s28, 0x10000
	v_mov_b32_e32 v7, s28
	v_mov_b32_e32 v19, 0
	v_mov_b32_e32 v20, 0
	v_mov_b32_e32 v21, 0
	v_mov_b32_e32 v22, 0
	s_waitcnt lgkmcnt(0)
	v_cmp_lt_u32_e64 s[32:33], 31, v8
	v_cmp_gt_u32_e64 s[34:35], 32, v8
	v_fma_mixlo_f16 v204, v188, s51, 0
	v_add_u32_e32 v167, 0, v165
	v_cmp_gt_u32_e32 vcc, 11, v167
	s_nop 1
	v_cndmask_b32_e32 v204, 0, v204, vcc
	v_fma_mixlo_f16 v205, v189, s51, 0
	v_add_u32_e32 v167, 1, v165
	v_cmp_gt_u32_e32 vcc, 11, v167
	s_nop 1
	v_cndmask_b32_e32 v205, 0, v205, vcc
	v_fma_mixlo_f16 v206, v190, s51, 0
	v_add_u32_e32 v167, 2, v165
	v_cmp_gt_u32_e32 vcc, 11, v167
	s_nop 1
	v_cndmask_b32_e32 v206, 0, v206, vcc
	v_fma_mixlo_f16 v207, v191, s51, 0
	v_add_u32_e32 v167, 3, v165
	v_cmp_gt_u32_e32 vcc, 11, v167
	s_nop 1
	v_cndmask_b32_e32 v207, 0, v207, vcc
	v_fma_mixlo_f16 v208, v192, s51, 0
	v_add_u32_e32 v167, 4, v165
	v_cmp_gt_u32_e32 vcc, 11, v167
	s_nop 1
	v_cndmask_b32_e32 v208, 0, v208, vcc
	v_fma_mixlo_f16 v209, v193, s51, 0
	v_add_u32_e32 v167, 5, v165
	v_cmp_gt_u32_e32 vcc, 11, v167
	s_nop 1
	v_cndmask_b32_e32 v209, 0, v209, vcc
	v_fma_mixlo_f16 v210, v194, s51, 0
	v_add_u32_e32 v167, 6, v165
	v_cmp_gt_u32_e32 vcc, 11, v167
	s_nop 1
	v_cndmask_b32_e32 v210, 0, v210, vcc
	v_fma_mixlo_f16 v211, v195, s51, 0
	v_add_u32_e32 v167, 7, v165
	v_cmp_gt_u32_e32 vcc, 11, v167
	s_nop 1
	v_cndmask_b32_e32 v211, 0, v211, vcc
	v_pack_b32_f16 v24, v204, v205
	v_pack_b32_f16 v25, v206, v207
	v_pack_b32_f16 v26, v208, v209
	v_pack_b32_f16 v27, v210, v211
	v_fma_mixlo_f16 v204, v196, s51, 0
	v_add_u32_e32 v167, 0, v166
	v_cmp_gt_u32_e32 vcc, 11, v167
	s_nop 1
	v_cndmask_b32_e32 v204, 0, v204, vcc
	v_fma_mixlo_f16 v205, v197, s51, 0
	v_add_u32_e32 v167, 1, v166
	v_cmp_gt_u32_e32 vcc, 11, v167
	s_nop 1
	v_cndmask_b32_e32 v205, 0, v205, vcc
	v_fma_mixlo_f16 v206, v198, s51, 0
	v_add_u32_e32 v167, 2, v166
	v_cmp_gt_u32_e32 vcc, 11, v167
	s_nop 1
	v_cndmask_b32_e32 v206, 0, v206, vcc
	v_fma_mixlo_f16 v207, v199, s51, 0
	v_add_u32_e32 v167, 3, v166
	v_cmp_gt_u32_e32 vcc, 11, v167
	s_nop 1
	v_cndmask_b32_e32 v207, 0, v207, vcc
	v_fma_mixlo_f16 v208, v200, s51, 0
	v_add_u32_e32 v167, 4, v166
	v_cmp_gt_u32_e32 vcc, 11, v167
	s_nop 1
	v_cndmask_b32_e32 v208, 0, v208, vcc
	v_fma_mixlo_f16 v209, v201, s51, 0
	v_add_u32_e32 v167, 5, v166
	v_cmp_gt_u32_e32 vcc, 11, v167
	s_nop 1
	v_cndmask_b32_e32 v209, 0, v209, vcc
	v_fma_mixlo_f16 v210, v202, s51, 0
	v_add_u32_e32 v167, 6, v166
	v_cmp_gt_u32_e32 vcc, 11, v167
	s_nop 1
	v_cndmask_b32_e32 v210, 0, v210, vcc
	v_fma_mixlo_f16 v211, v203, s51, 0
	v_add_u32_e32 v167, 7, v166
	v_cmp_gt_u32_e32 vcc, 11, v167
	s_nop 1
	v_cndmask_b32_e32 v211, 0, v211, vcc
	v_pack_b32_f16 v167, v204, v205
	v_cndmask_b32_e64 v28, 0, v167, s[32:33]
	v_cndmask_b32_e64 v32, 0, v167, s[34:35]
	v_pack_b32_f16 v167, v206, v207
	v_cndmask_b32_e64 v29, 0, v167, s[32:33]
	v_cndmask_b32_e64 v33, 0, v167, s[34:35]
	v_pack_b32_f16 v167, v208, v209
	v_cndmask_b32_e64 v30, 0, v167, s[32:33]
	v_cndmask_b32_e64 v34, 0, v167, s[34:35]
	v_pack_b32_f16 v167, v210, v211
	v_cndmask_b32_e64 v31, 0, v167, s[32:33]
	v_cndmask_b32_e64 v35, 0, v167, s[34:35]
	s_waitcnt lgkmcnt(0)
	s_cmp_lt_u32 s12, 4
	s_cbranch_scc1 .Lq_noprio
	s_setprio 1
.Lq_noprio:
	s_waitcnt vmcnt(28)
	v_cvt_pk_f16_f32 v164, v36, v40
	v_cvt_pk_f16_f32 v180, v68, v72
	v_pk_add_f16 v164, v164, -0.5 op_sel_hi:[1,0]
	v_pk_add_f16 v180, v180, -0.5 op_sel_hi:[1,0]
	v_pk_mul_f16 v196, v180, v180
	v_pk_mul_f16 v212, v164, v180
	v_pk_fma_f16 v196, v164, v164, v196
	v_cvt_pk_f16_f32 v168, v37, v41
	v_cvt_pk_f16_f32 v184, v69, v73
	v_pk_add_f16 v168, v168, -0.5 op_sel_hi:[1,0]
	v_pk_add_f16 v184, v184, -0.5 op_sel_hi:[1,0]
	v_pk_mul_f16 v200, v184, v184
	v_pk_mul_f16 v216, v168, v184
	v_pk_fma_f16 v200, v168, v168, v200
	v_cvt_pk_f16_f32 v172, v38, v42
	v_cvt_pk_f16_f32 v188, v70, v74
	v_pk_add_f16 v172, v172, -0.5 op_sel_hi:[1,0]
	v_pk_add_f16 v188, v188, -0.5 op_sel_hi:[1,0]
	v_pk_mul_f16 v204, v188, v188
	v_pk_mul_f16 v220, v172, v188
	v_pk_fma_f16 v204, v172, v172, v204
	v_cvt_pk_f16_f32 v176, v39, v43
	v_cvt_pk_f16_f32 v192, v71, v75
	v_pk_add_f16 v176, v176, -0.5 op_sel_hi:[1,0]
	v_pk_add_f16 v192, v192, -0.5 op_sel_hi:[1,0]
	v_pk_mul_f16 v208, v192, v192
	v_pk_mul_f16 v224, v176, v192
	v_pk_fma_f16 v208, v176, v176, v208
	s_waitcnt vmcnt(24)
	v_cvt_pk_f16_f32 v165, v44, v48
	v_cvt_pk_f16_f32 v181, v76, v80
	v_pk_add_f16 v165, v165, -0.5 op_sel_hi:[1,0]
	v_pk_add_f16 v181, v181, -0.5 op_sel_hi:[1,0]
	v_pk_mul_f16 v197, v181, v181
	v_pk_mul_f16 v213, v165, v181
	v_pk_fma_f16 v197, v165, v165, v197
	v_cvt_pk_f16_f32 v169, v45, v49
	v_cvt_pk_f16_f32 v185, v77, v81
	v_pk_add_f16 v169, v169, -0.5 op_sel_hi:[1,0]
	v_pk_add_f16 v185, v185, -0.5 op_sel_hi:[1,0]
	v_pk_mul_f16 v201, v185, v185
	v_pk_mul_f16 v217, v169, v185
	v_pk_fma_f16 v201, v169, v169, v201
	v_cvt_pk_f16_f32 v173, v46, v50
	v_cvt_pk_f16_f32 v189, v78, v82
	v_pk_add_f16 v173, v173, -0.5 op_sel_hi:[1,0]
	v_pk_add_f16 v189, v189, -0.5 op_sel_hi:[1,0]
	v_pk_mul_f16 v205, v189, v189
	v_pk_mul_f16 v221, v173, v189
	v_pk_fma_f16 v205, v173, v173, v205
	v_cvt_pk_f16_f32 v177, v47, v51
	v_cvt_pk_f16_f32 v193, v79, v83
	v_pk_add_f16 v177, v177, -0.5 op_sel_hi:[1,0]
	v_pk_add_f16 v193, v193, -0.5 op_sel_hi:[1,0]
	v_pk_mul_f16 v209, v193, v193
	v_pk_mul_f16 v225, v177, v193
	v_pk_fma_f16 v209, v177, v177, v209
	s_waitcnt vmcnt(20)
	v_cvt_pk_f16_f32 v166, v52, v56
	v_cvt_pk_f16_f32 v182, v84, v88
	v_pk_add_f16 v166, v166, -0.5 op_sel_hi:[1,0]
	v_pk_add_f16 v182, v182, -0.5 op_sel_hi:[1,0]
	v_pk_mul_f16 v198, v182, v182
	v_pk_mul_f16 v214, v166, v182
	v_pk_fma_f16 v198, v166, v166, v198
	v_cvt_pk_f16_f32 v170, v53, v57
	v_cvt_pk_f16_f32 v186, v85, v89
	v_pk_add_f16 v170, v170, -0.5 op_sel_hi:[1,0]
	v_pk_add_f16 v186, v186, -0.5 op_sel_hi:[1,0]
	v_pk_mul_f16 v202, v186, v186
	v_pk_mul_f16 v218, v170, v186
	v_pk_fma_f16 v202, v170, v170, v202
	v_cvt_pk_f16_f32 v174, v54, v58
	v_cvt_pk_f16_f32 v190, v86, v90
	v_pk_add_f16 v174, v174, -0.5 op_sel_hi:[1,0]
	v_pk_add_f16 v190, v190, -0.5 op_sel_hi:[1,0]
	v_pk_mul_f16 v206, v190, v190
	v_pk_mul_f16 v222, v174, v190
	v_pk_fma_f16 v206, v174, v174, v206
	v_cvt_pk_f16_f32 v178, v55, v59
	v_cvt_pk_f16_f32 v194, v87, v91
	v_pk_add_f16 v178, v178, -0.5 op_sel_hi:[1,0]
	v_pk_add_f16 v194, v194, -0.5 op_sel_hi:[1,0]
	v_pk_mul_f16 v210, v194, v194
	v_pk_mul_f16 v226, v178, v194
	v_pk_fma_f16 v210, v178, v178, v210
	s_waitcnt vmcnt(16)
	v_cvt_pk_f16_f32 v167, v60, v64
	v_cvt_pk_f16_f32 v183, v92, v96
	v_pk_add_f16 v167, v167, -0.5 op_sel_hi:[1,0]
	v_pk_add_f16 v183, v183, -0.5 op_sel_hi:[1,0]
	v_pk_mul_f16 v199, v183, v183
	v_pk_mul_f16 v215, v167, v183
	v_pk_fma_f16 v199, v167, v167, v199
	v_cvt_pk_f16_f32 v171, v61, v65
	v_cvt_pk_f16_f32 v187, v93, v97
	v_pk_add_f16 v171, v171, -0.5 op_sel_hi:[1,0]
	v_pk_add_f16 v187, v187, -0.5 op_sel_hi:[1,0]
	v_pk_mul_f16 v203, v187, v187
	v_pk_mul_f16 v219, v171, v187
	v_pk_fma_f16 v203, v171, v171, v203
	v_cvt_pk_f16_f32 v175, v62, v66
	v_cvt_pk_f16_f32 v191, v94, v98
	v_pk_add_f16 v175, v175, -0.5 op_sel_hi:[1,0]
	v_pk_add_f16 v191, v191, -0.5 op_sel_hi:[1,0]
	v_pk_mul_f16 v207, v191, v191
	v_pk_mul_f16 v223, v175, v191
	v_pk_fma_f16 v207, v175, v175, v207
	v_cvt_pk_f16_f32 v179, v63, v67
	v_cvt_pk_f16_f32 v195, v95, v99
	v_pk_add_f16 v179, v179, -0.5 op_sel_hi:[1,0]
	v_pk_add_f16 v195, v195, -0.5 op_sel_hi:[1,0]
	v_pk_mul_f16 v211, v195, v195
	v_pk_mul_f16 v227, v179, v195
	v_pk_fma_f16 v211, v179, v179, v211
	v_mfma_f32_16x16x32_f16 v[68:71], v[164:167], v[24:27], 0
	v_mfma_f32_16x16x32_f16 v[72:75], v[168:171], v[24:27], 0
	v_mfma_f32_16x16x32_f16 v[76:79], v[172:175], v[24:27], 0
	v_mfma_f32_16x16x32_f16 v[80:83], v[176:179], v[24:27], 0
	v_mfma_f32_16x16x32_f16 v[84:87], v[180:183], v[24:27], 0
	v_mfma_f32_16x16x32_f16 v[88:91], v[184:187], v[24:27], 0
	v_mfma_f32_16x16x32_f16 v[92:95], v[188:191], v[24:27], 0
	v_mfma_f32_16x16x32_f16 v[96:99], v[192:195], v[24:27], 0
	s_nop 1
	v_cvt_pk_f16_f32 v36, v68, v72
	s_nop 0
	v_cvt_pk_f16_f32 v37, v76, v80
	v_cvt_pk_f16_f32 v38, v69, v73
	v_cvt_pk_f16_f32 v39, v77, v81
	v_cvt_pk_f16_f32 v40, v70, v74
	v_cvt_pk_f16_f32 v41, v78, v82
	v_cvt_pk_f16_f32 v42, v71, v75
	v_cvt_pk_f16_f32 v43, v79, v83
	v_mfma_f32_16x16x32_f16 v[68:71], v[196:199], v[24:27], 0
	v_mfma_f32_16x16x32_f16 v[72:75], v[200:203], v[24:27], 0
	v_mfma_f32_16x16x32_f16 v[76:79], v[204:207], v[24:27], 0
	v_mfma_f32_16x16x32_f16 v[80:83], v[208:211], v[24:27], 0
	v_cvt_pk_f16_f32 v44, v84, v88
	v_cvt_pk_f16_f32 v45, v92, v96
	v_cvt_pk_f16_f32 v46, v85, v89
	v_cvt_pk_f16_f32 v47, v93, v97
	v_cvt_pk_f16_f32 v48, v86, v90
	v_cvt_pk_f16_f32 v49, v94, v98
	v_cvt_pk_f16_f32 v50, v87, v91
	v_cvt_pk_f16_f32 v51, v95, v99
	v_mfma_f32_16x16x32_f16 v[84:87], v[212:215], v[24:27], 0
	v_mfma_f32_16x16x32_f16 v[88:91], v[216:219], v[24:27], 0
	v_mfma_f32_16x16x32_f16 v[92:95], v[220:223], v[24:27], 0
	v_mfma_f32_16x16x32_f16 v[96:99], v[224:227], v[24:27], 0
	v_cvt_pk_f16_f32 v52, v68, v72
	v_cvt_pk_f16_f32 v53, v76, v80
	v_cvt_pk_f16_f32 v54, v69, v73
	v_cvt_pk_f16_f32 v55, v77, v81
	v_cvt_pk_f16_f32 v56, v70, v74
	v_cvt_pk_f16_f32 v57, v78, v82
	v_cvt_pk_f16_f32 v58, v71, v75
	v_cvt_pk_f16_f32 v59, v79, v83
	v_cvt_pk_f16_f32 v60, v84, v88
	v_cvt_pk_f16_f32 v61, v92, v96
	v_cvt_pk_f16_f32 v62, v85, v89
	v_cvt_pk_f16_f32 v63, v93, v97
	v_cvt_pk_f16_f32 v64, v86, v90
	v_cvt_pk_f16_f32 v65, v94, v98
	v_cvt_pk_f16_f32 v66, v87, v91
	v_cvt_pk_f16_f32 v67, v95, v99
	s_mov_b64 exec, s[38:39]
	ds_write_b128 v4, v[40:43] offset:0
	ds_write_b128 v4, v[48:51] offset:512
	ds_write_b128 v4, v[56:59] offset:1024
	ds_write_b128 v4, v[64:67] offset:1536
	s_mov_b64 exec, -1
	v_mfma_f32_16x16x32_f16 v[68:71], v[24:27], v[36:39], 0
	v_mfma_f32_16x16x32_f16 v[72:75], v[24:27], v[44:47], 0
	v_mfma_f32_16x16x32_f16 v[76:79], v[24:27], v[52:55], v[0:3]
	v_mfma_f32_16x16x32_f16 v[80:83], v[24:27], v[60:63], 0
	v_mfma_f32_16x16x32_f16 v[84:87], v[28:31], v[36:39], 0
	v_mfma_f32_16x16x32_f16 v[88:91], v[28:31], v[44:47], 0
	v_mfma_f32_16x16x32_f16 v[92:95], v[28:31], v[52:55], v[0:3]
	v_mfma_f32_16x16x32_f16 v[96:99], v[28:31], v[60:63], 0
	v_mfma_f32_16x16x32_f16 v[84:87], v[32:35], v[40:43], v[84:87]
	v_mfma_f32_16x16x32_f16 v[88:91], v[32:35], v[48:51], v[88:91]
	v_mfma_f32_16x16x32_f16 v[92:95], v[32:35], v[56:59], v[92:95]
	v_mfma_f32_16x16x32_f16 v[96:99], v[32:35], v[64:67], v[96:99]
	s_waitcnt lgkmcnt(0)
	ds_write_b32 v6, v6 offset:0
	ds_read_b32 v9, v7 offset:0
	v_mul_f32_e32 v244, v68, v72
	v_mul_f32_e32 v250, v69, v73
	v_mul_f32_e64 v245, -v72, v72
	v_mul_f32_e64 v251, -v73, v73
	v_add_f32_e32 v246, v68, v72
	v_add_f32_e32 v252, v69, v73
	v_fma_f32 v245, -v68, v68, v245
	v_fma_f32 v251, -v69, v69, v251
	v_fma_f32 v247, v10, v246, v11
	v_fma_f32 v253, v10, v252, v11
	v_fma_f32 v246, v13, v80, v14
	v_fma_f32 v252, v13, v81, v14
	v_fma_f32 v248, v12, v76, v245
	v_fma_f32 v254, v12, v77, v251
	v_fma_f32 v249, 2.0, v244, v247
	v_fma_f32 v255, 2.0, v250, v253
	v_sub_f32_e32 v247, v247, v245
	v_sub_f32_e32 v253, v253, v251
	v_fma_f32 v246, -2.0, v244, v246
	v_fma_f32 v252, -2.0, v250, v252
	v_mul_f32_e32 v247, v247, v248
	v_mul_f32_e32 v253, v253, v254
	v_rcp_f32_e32 v247, v247
	v_rcp_f32_e32 v253, v253
	v_mul_f32_e32 v249, v249, v246
	v_mul_f32_e32 v255, v255, v252
	v_fma_f32 v19, v249, v247, v19
	v_fma_f32 v19, v255, v253, v19
	v_mul_f32_e32 v244, v70, v74
	v_mul_f32_e32 v250, v71, v75
	v_mul_f32_e64 v245, -v74, v74
	v_mul_f32_e64 v251, -v75, v75
	v_add_f32_e32 v246, v70, v74
	v_add_f32_e32 v252, v71, v75
	v_fma_f32 v245, -v70, v70, v245
	v_fma_f32 v251, -v71, v71, v251
	v_fma_f32 v247, v10, v246, v11
	v_fma_f32 v253, v10, v252, v11
	v_fma_f32 v246, v13, v82, v14
	v_fma_f32 v252, v13, v83, v14
	v_fma_f32 v248, v12, v78, v245
	v_fma_f32 v254, v12, v79, v251
	v_fma_f32 v249, 2.0, v244, v247
	v_fma_f32 v255, 2.0, v250, v253
	v_sub_f32_e32 v247, v247, v245
	v_sub_f32_e32 v253, v253, v251
	v_fma_f32 v246, -2.0, v244, v246
	v_fma_f32 v252, -2.0, v250, v252
	v_mul_f32_e32 v247, v247, v248
	v_mul_f32_e32 v253, v253, v254
	v_rcp_f32_e32 v247, v247
	v_rcp_f32_e32 v253, v253
	v_mul_f32_e32 v249, v249, v246
	v_mul_f32_e32 v255, v255, v252
	v_fma_f32 v20, v249, v247, v20
	v_fma_f32 v20, v255, v253, v20
	v_mfma_f32_16x16x32_f16 v[68:71], v[24:27], v[40:43], 0
	v_mfma_f32_16x16x32_f16 v[72:75], v[24:27], v[48:51], 0
	v_mfma_f32_16x16x32_f16 v[76:79], v[24:27], v[56:59], v[0:3]
	v_mfma_f32_16x16x32_f16 v[80:83], v[24:27], v[64:67], 0
	s_barrier
	ds_read_b32 v9, v7 offset:0
	s_waitcnt lgkmcnt(0)
	v_cmp_ne_u32_e32 vcc, 0, v9
	s_cbranch_vccnz .Lq_go_0
